# superstack: g2p + W_xq loop prefetch + pass-2 read-back via LDS + cvt_pk packs in phase 0
# speedup vs baseline: 1.0003x; 1.0003x over previous
; __device__ __forceinline__ unsigned pk2(float lo, float hi) { return f2bf(lo) | (f2bf(hi) << 16); }
; #define INP(k) ldptr(PTAB, (k))
; __global__ void __launch_bounds__(NWAVES * 64, 2) fwd_kernel(Args args) {
;     ...
;             { const float* wq = INP(19) + (size_t)l * D * D; const float* gq = INP(17) + l * D;
;               for (int i = gw * 64 + lane; i < D * D / 8; i += ngw * 64) { const f32x4 a = *(const f32x4*)(wq + (size_t)i * 8), bq = *(const f32x4*)(wq + (size_t)i * 8 + 4); const float gg = gq[i >> 8];
;                   v4u o; o.x = pk2(a.x * gg, a.y * gg); o.y = pk2(a.z * gg, a.w * gg); o.z = pk2(bq.x * gg, bq.y * gg); o.w = pk2(bq.z * gg, bq.w * gg); ((v4u*)WSP(WS_WXQ))[i] = o; } }
.LBB0_490:
	v_ashrrev_i32_e32 v60, 8, v0
	v_ashrrev_i32_e32 v61, 31, v60
	global_load_dwordx4 v[40:43], v[4:5], off offset:-16
	global_load_dwordx4 v[80:83], v[4:5], off
	v_lshl_add_u64 v[60:61], v[60:61], 2, s[4:5]
	global_load_dword v56, v[60:61], off
	v_add_u32_e32 v0, s82, v0
	v_lshl_add_u64 v[4:5], v[4:5], 0, s[88:89]
	v_ashrrev_i32_e32 v60, 8, v0
	v_ashrrev_i32_e32 v61, 31, v60
	global_load_dwordx4 v[44:47], v[4:5], off offset:-16
	global_load_dwordx4 v[84:87], v[4:5], off
	v_lshl_add_u64 v[60:61], v[60:61], 2, s[4:5]
	global_load_dword v57, v[60:61], off
	v_add_u32_e32 v0, s82, v0
	v_lshl_add_u64 v[4:5], v[4:5], 0, s[88:89]
	v_ashrrev_i32_e32 v60, 8, v0
	v_ashrrev_i32_e32 v61, 31, v60
	global_load_dwordx4 v[48:51], v[4:5], off offset:-16
	global_load_dwordx4 v[88:91], v[4:5], off
	v_lshl_add_u64 v[60:61], v[60:61], 2, s[4:5]
	global_load_dword v58, v[60:61], off
	v_add_u32_e32 v0, s82, v0
	v_lshl_add_u64 v[4:5], v[4:5], 0, s[88:89]
	v_ashrrev_i32_e32 v60, 8, v0
	v_ashrrev_i32_e32 v61, 31, v60
	global_load_dwordx4 v[52:55], v[4:5], off offset:-16
	global_load_dwordx4 v[92:95], v[4:5], off
	v_lshl_add_u64 v[60:61], v[60:61], 2, s[4:5]
	global_load_dword v59, v[60:61], off
	v_add_u32_e32 v0, s82, v0
	v_lshl_add_u64 v[4:5], v[4:5], 0, s[88:89]
	s_waitcnt vmcnt(9)
	v_mov_b32_e32 v6, v40
	v_mov_b32_e32 v7, v41
	v_mov_b32_e32 v8, v42
	v_mov_b32_e32 v9, v43
	v_mov_b32_e32 v10, v80
	v_mov_b32_e32 v11, v81
	v_mov_b32_e32 v12, v82
	v_mov_b32_e32 v13, v83
	v_mov_b32_e32 v14, v56
	v_mov_b32_e32 v16, v6
	v_mov_b32_e32 v17, v8
	v_mov_b32_e32 v8, v7
	v_mov_b32_e32 v6, v10
	v_mov_b32_e32 v7, v12
	v_mov_b32_e32 v12, v11
	v_pk_mul_f32 v[10:11], v[16:17], v[14:15] op_sel_hi:[1,0]
	v_pk_mul_f32 v[6:7], v[6:7], v[14:15] op_sel_hi:[1,0]
	v_pk_mul_f32 v[8:9], v[8:9], v[14:15] op_sel_hi:[1,0]
	v_pk_mul_f32 v[12:13], v[12:13], v[14:15] op_sel_hi:[1,0]
	v_bfe_u32 v18, v10, 16, 1
	v_bfe_u32 v19, v11, 16, 1
	v_bfe_u32 v20, v6, 16, 1
	v_bfe_u32 v15, v12, 16, 1
	v_bfe_u32 v16, v9, 16, 1
	v_bfe_u32 v17, v8, 16, 1
	v_add3_u32 v6, v6, v20, s40
	v_add3_u32 v11, v11, v19, s40
	v_add3_u32 v10, v10, v18, s40
	v_add3_u32 v17, v8, v17, s40
	v_add3_u32 v16, v9, v16, s40
	v_add3_u32 v8, v12, v15, s40
	v_lshrrev_b32_e32 v10, 16, v10
	v_lshrrev_b32_e32 v11, 16, v11
	v_lshrrev_b32_e32 v6, 16, v6
	v_cvt_pk_bf16_f32 v9, v7, v13
	v_and_or_b32 v8, v8, s41, v6
	v_and_or_b32 v7, v16, s41, v11
	v_and_or_b32 v6, v17, s41, v10
	global_store_dwordx4 v[2:3], v[6:9], off
	v_lshl_add_u64 v[2:3], v[2:3], 0, s[86:87]
	s_nop 1
	s_waitcnt vmcnt(6)
	v_mov_b32_e32 v6, v44
	v_mov_b32_e32 v7, v45
	v_mov_b32_e32 v8, v46
	v_mov_b32_e32 v9, v47
	v_mov_b32_e32 v10, v84
	v_mov_b32_e32 v11, v85
	v_mov_b32_e32 v12, v86
	v_mov_b32_e32 v13, v87
	v_mov_b32_e32 v14, v57
	v_mov_b32_e32 v16, v6
	v_mov_b32_e32 v17, v8
	v_mov_b32_e32 v8, v7
	v_mov_b32_e32 v6, v10
	v_mov_b32_e32 v7, v12
	v_mov_b32_e32 v12, v11
	v_pk_mul_f32 v[10:11], v[16:17], v[14:15] op_sel_hi:[1,0]
	v_pk_mul_f32 v[6:7], v[6:7], v[14:15] op_sel_hi:[1,0]
	v_pk_mul_f32 v[8:9], v[8:9], v[14:15] op_sel_hi:[1,0]
	v_pk_mul_f32 v[12:13], v[12:13], v[14:15] op_sel_hi:[1,0]
	v_bfe_u32 v18, v10, 16, 1
	v_bfe_u32 v19, v11, 16, 1
	v_bfe_u32 v20, v6, 16, 1
	v_bfe_u32 v15, v12, 16, 1
	v_bfe_u32 v16, v9, 16, 1
	v_bfe_u32 v17, v8, 16, 1
	v_add3_u32 v6, v6, v20, s40
	v_add3_u32 v11, v11, v19, s40
	v_add3_u32 v10, v10, v18, s40
	v_add3_u32 v17, v8, v17, s40
	v_add3_u32 v16, v9, v16, s40
	v_add3_u32 v8, v12, v15, s40
	v_lshrrev_b32_e32 v10, 16, v10
	v_lshrrev_b32_e32 v11, 16, v11
	v_lshrrev_b32_e32 v6, 16, v6
	v_cvt_pk_bf16_f32 v9, v7, v13
	v_and_or_b32 v8, v8, s41, v6
	v_and_or_b32 v7, v16, s41, v11
	v_and_or_b32 v6, v17, s41, v10
	global_store_dwordx4 v[2:3], v[6:9], off
	v_lshl_add_u64 v[2:3], v[2:3], 0, s[86:87]
	s_nop 1
	s_waitcnt vmcnt(3)
	v_mov_b32_e32 v6, v48
	v_mov_b32_e32 v7, v49
	v_mov_b32_e32 v8, v50
	v_mov_b32_e32 v9, v51
	v_mov_b32_e32 v10, v88
	v_mov_b32_e32 v11, v89
	v_mov_b32_e32 v12, v90
	v_mov_b32_e32 v13, v91
	v_mov_b32_e32 v14, v58
	v_mov_b32_e32 v16, v6
	v_mov_b32_e32 v17, v8
	v_mov_b32_e32 v8, v7
	v_mov_b32_e32 v6, v10
	v_mov_b32_e32 v7, v12
	v_mov_b32_e32 v12, v11
	v_pk_mul_f32 v[10:11], v[16:17], v[14:15] op_sel_hi:[1,0]
	v_pk_mul_f32 v[6:7], v[6:7], v[14:15] op_sel_hi:[1,0]
	v_pk_mul_f32 v[8:9], v[8:9], v[14:15] op_sel_hi:[1,0]
	v_pk_mul_f32 v[12:13], v[12:13], v[14:15] op_sel_hi:[1,0]
	v_bfe_u32 v18, v10, 16, 1
	v_bfe_u32 v19, v11, 16, 1
	v_bfe_u32 v20, v6, 16, 1
	v_bfe_u32 v15, v12, 16, 1
	v_bfe_u32 v16, v9, 16, 1
	v_bfe_u32 v17, v8, 16, 1
	v_add3_u32 v6, v6, v20, s40
	v_add3_u32 v11, v11, v19, s40
	v_add3_u32 v10, v10, v18, s40
	v_add3_u32 v17, v8, v17, s40
	v_add3_u32 v16, v9, v16, s40
	v_add3_u32 v8, v12, v15, s40
	v_lshrrev_b32_e32 v10, 16, v10
	v_lshrrev_b32_e32 v11, 16, v11
	v_lshrrev_b32_e32 v6, 16, v6
	v_cvt_pk_bf16_f32 v9, v7, v13
	v_and_or_b32 v8, v8, s41, v6
	v_and_or_b32 v7, v16, s41, v11
	v_and_or_b32 v6, v17, s41, v10
	global_store_dwordx4 v[2:3], v[6:9], off
	v_lshl_add_u64 v[2:3], v[2:3], 0, s[86:87]
	s_nop 1
	s_waitcnt vmcnt(0)
	v_mov_b32_e32 v6, v52
	v_mov_b32_e32 v7, v53
	v_mov_b32_e32 v8, v54
	v_mov_b32_e32 v9, v55
	v_mov_b32_e32 v10, v92
	v_mov_b32_e32 v11, v93
	v_mov_b32_e32 v12, v94
	v_mov_b32_e32 v13, v95
	v_mov_b32_e32 v14, v59
	v_mov_b32_e32 v16, v6
	v_mov_b32_e32 v17, v8
	v_mov_b32_e32 v8, v7
	v_mov_b32_e32 v6, v10
	v_mov_b32_e32 v7, v12
	v_mov_b32_e32 v12, v11
	v_pk_mul_f32 v[10:11], v[16:17], v[14:15] op_sel_hi:[1,0]
	v_pk_mul_f32 v[6:7], v[6:7], v[14:15] op_sel_hi:[1,0]
	v_pk_mul_f32 v[8:9], v[8:9], v[14:15] op_sel_hi:[1,0]
	v_pk_mul_f32 v[12:13], v[12:13], v[14:15] op_sel_hi:[1,0]
	v_bfe_u32 v18, v10, 16, 1
	v_bfe_u32 v19, v11, 16, 1
	v_bfe_u32 v20, v6, 16, 1
	v_bfe_u32 v15, v12, 16, 1
	v_bfe_u32 v16, v9, 16, 1
	v_bfe_u32 v17, v8, 16, 1
	v_add3_u32 v6, v6, v20, s40
	v_add3_u32 v11, v11, v19, s40
	v_add3_u32 v10, v10, v18, s40
	v_add3_u32 v17, v8, v17, s40
	v_add3_u32 v16, v9, v16, s40
	v_add3_u32 v8, v12, v15, s40
	v_lshrrev_b32_e32 v10, 16, v10
	v_lshrrev_b32_e32 v11, 16, v11
	v_lshrrev_b32_e32 v6, 16, v6
	v_cvt_pk_bf16_f32 v9, v7, v13
	v_and_or_b32 v8, v8, s41, v6
	v_and_or_b32 v7, v16, s41, v11
	v_and_or_b32 v6, v17, s41, v10
	global_store_dwordx4 v[2:3], v[6:9], off
	v_lshl_add_u64 v[2:3], v[2:3], 0, s[86:87]
